# v68 + 64-byte alignment of phase entry points
# speedup vs baseline: 1.0151x; 1.0085x over previous
.Lg_nocopy:
	v_and_b32_e32 v138, 15, v0
	v_or_b32_e32 v134, s24, v138
	v_lshlrev_b32_e32 v135, 3, v1
	v_lshlrev_b32_e32 v139, 2, v1
	v_bfe_u32 v140, v0, 4, 2
	v_cmp_eq_u32_e64 s[2:3], 0, v1
	.p2align 6

.LBB0_145:
	s_mov_b32 s25, 0
	s_lshr_b32 s24, s9, 16
	s_and_b32 s6, s7, 0xffff0000
	s_mov_b32 s7, s25
	s_lshr_b64 s[4:5], s[4:5], 16
	s_or_b64 s[6:7], s[6:7], s[24:25]
	s_mov_b32 s4, s25
	s_or_b64 s[4:5], s[6:7], s[4:5]
	s_and_b32 s7, s1, 0xffff0000
	s_mov_b32 s6, s25
	s_or_b64 s[6:7], s[4:5], s[6:7]
	s_add_u32 s4, s6, -1
	s_addc_u32 s5, s7, -1
	s_and_b64 s[4:5], s[6:7], s[4:5]
	s_cmp_eq_u64 s[4:5], 0
	v_readlane_b32 s4, v14, 48
	s_cbranch_scc0 .Lslowout_3
	.p2align 6
